# P7: a head's sub-key rows staged into LDS with all 8 loads in flight instead of 8 load+wait round trips
# speedup vs baseline: 1.0423x; 1.0034x over previous
; #define GAS __attribute__((address_space(1)))
; #define LAS __attribute__((address_space(3)))
; __device__ __forceinline__ f32x4 mfma16(bf16x8 a, bf16x8 b, f32x4 c) { return __builtin_amdgcn_mfma_f32_16x16x32_bf16(a, b, c, 0, 0, 0); }
; __device__ __forceinline__ void topk_task(const Frame& F, int l, int tb, int h, const LAS unsigned char* kl, LAS float* tl, const LAS unsigned char* cab) {
;     ...
;     bf16x8 Qall[2][4];
; #pragma unroll
;     for (int p = 0; p < 2; ++p)
; #pragma unroll
;         for (int ks = 0; ks < 4; ++ks) Qall[p][ks] = ld_b8(QP + (size_t)(t0 + c) * QPP + h * 256 + p * 128 + ks * 32 + rq * 8);
;     float rsp[8];
;     { const float* SS2 = (const float*)(F.ws + WS_SS2) + (t0 + c);
; #pragma unroll
;         for (int i = 0; i < 8; ++i) rsp[i] = *(const GAS float*)(SS2 + (size_t)(rq * 8 + i) * T); }
; #pragma unroll
;     for (int p = 0; p < 2; ++p) {
;         bf16x8 Qf[4];
; #pragma unroll
;         for (int ks = 0; ks < 4; ++ks) Qf[ks] = Qall[p][ks];
;         float v[32];
;         const LAS unsigned char* kbase = kl + (p * 128 + c) * KL_PITCH + rq * 16;
; #pragma unroll
;         for (int kb = 0; kb < 8; ++kb) {
;             f32x4 a = (f32x4){0.f, 0.f, 0.f, 0.f};
; #pragma unroll
;             for (int ks = 0; ks < 4; ++ks) a = mfma16(*(const LAS bf16x8*)(kbase + kb * 16 * KL_PITCH + ks * 64), Qf[ks], a);
; __global__ void __launch_bounds__(NWAVES * 64, 2) hybrid_fwd(Args args) {
;     ...
;                     __syncthreads();
; #pragma unroll
;                     for (int i = 0; i < 8; ++i) { const int idx = tid3 + 512 * i, row = idx >> 4, c16 = idx & 15;
;                         *(LAS u32x4*)(kl + row * KL_PITCH + c16 * 16) = ld_u4(KEYS + ((size_t)h * 256 + row) * 128 + c16 * 8); }
;                     __syncthreads();
.LBB0_1009:
	v_lshl_add_u64 v[32:33], s[62:63], 0, v[66:67]
	v_add_co_u32_e32 v32, vcc, 0x300000, v32
	s_nop 1
	v_addc_co_u32_e32 v33, vcc, 0, v33, vcc
	s_barrier
	global_load_dwordx4 v[0:3], v[32:33], off
	v_mov_b32_e32 v90, v211
	v_lshl_add_u64 v[32:33], s[62:63], 0, v[64:65]
	v_add_co_u32_e32 v32, vcc, 0x300000, v32
	s_nop 1
	v_addc_co_u32_e32 v33, vcc, 0, v33, vcc
	global_load_dwordx4 v[4:7], v[32:33], off
	v_lshl_add_u64 v[32:33], s[62:63], 0, v[62:63]
	v_add_co_u32_e32 v32, vcc, 0x300000, v32
	s_nop 1
	v_addc_co_u32_e32 v33, vcc, 0, v33, vcc
	global_load_dwordx4 v[8:11], v[32:33], off
	v_lshl_add_u64 v[32:33], s[62:63], 0, v[60:61]
	v_add_co_u32_e32 v32, vcc, 0x300000, v32
	s_nop 1
	v_addc_co_u32_e32 v33, vcc, 0, v33, vcc
	global_load_dwordx4 v[12:15], v[32:33], off
	v_lshl_add_u64 v[32:33], s[62:63], 0, v[58:59]
	v_add_co_u32_e32 v32, vcc, 0x300000, v32
	s_nop 1
	v_addc_co_u32_e32 v33, vcc, 0, v33, vcc
	global_load_dwordx4 v[16:19], v[32:33], off
	v_lshl_add_u64 v[32:33], s[62:63], 0, v[56:57]
	v_add_co_u32_e32 v32, vcc, 0x300000, v32
	s_nop 1
	v_addc_co_u32_e32 v33, vcc, 0, v33, vcc
	global_load_dwordx4 v[20:23], v[32:33], off
	v_lshl_add_u64 v[32:33], s[62:63], 0, v[54:55]
	v_add_co_u32_e32 v32, vcc, 0x300000, v32
	s_nop 1
	v_addc_co_u32_e32 v33, vcc, 0, v33, vcc
	global_load_dwordx4 v[24:27], v[32:33], off
	v_lshl_add_u64 v[32:33], s[62:63], 0, v[52:53]
	v_add_co_u32_e32 v32, vcc, 0x300000, v32
	s_nop 1
	v_addc_co_u32_e32 v33, vcc, 0, v33, vcc
	global_load_dwordx4 v[28:31], v[32:33], off
	s_waitcnt vmcnt(0)
	ds_write_b128 v72, v[0:3]
	ds_write_b128 v73, v[4:7]
	ds_write_b128 v74, v[8:11]
	ds_write_b128 v75, v[12:15]
	ds_write_b128 v76, v[16:19]
	ds_write_b128 v77, v[20:23]
	ds_write_b128 v78, v[24:27]
	ds_write_b128 v79, v[28:31]
	s_waitcnt lgkmcnt(0)
	s_barrier
	s_nop 0
	v_ashrrev_i32_e32 v80, 4, v90
	v_lshlrev_b32_e32 v34, 3, v80
	v_and_b32_e32 v88, 15, v90
	v_ashrrev_i32_e32 v35, 31, v34
	v_add_u32_e32 v68, s24, v88
	v_lshlrev_b64 v[0:1], 1, v[34:35]
	v_mad_i64_i32 v[0:1], s[0:1], v68, s33, v[0:1]
	s_add_u32 s0, s62, s17
	s_addc_u32 s1, s63, s22
	v_lshl_add_u64 v[0:1], s[0:1], 0, v[0:1]
	s_mov_b32 s0, 0x32c00000
	v_add_co_u32_e32 v0, vcc, s0, v0
	v_or_b32_e32 v32, s23, v88
	s_nop 0
	v_addc_co_u32_e32 v1, vcc, 0, v1, vcc
	v_lshlrev_b32_e32 v226, 4, v88
	v_lshl_add_u32 v226, v80, 8, v226
	v_lshl_add_u32 v226, s24, 12, v226
	v_lshl_add_u32 v226, s17, 4, v226
	v_add_u32_e32 v226, 0x32c00000, v226
	v_mov_b32_e32 v227, 0
	v_lshl_add_u64 v[0:1], s[62:63], 0, v[226:227]
	v_mov_b32_e32 v226, 0x1000
	v_lshl_add_u64 v[228:229], v[0:1], 0, v[226:227]
	global_load_dwordx4 v[28:31], v[0:1], off
	global_load_dwordx4 v[24:27], v[0:1], off offset:1024
	global_load_dwordx4 v[20:23], v[0:1], off offset:2048
	global_load_dwordx4 v[16:19], v[0:1], off offset:3072
	global_load_dwordx4 v[12:15], v[228:229], off
	global_load_dwordx4 v[8:11], v[228:229], off offset:1024
	global_load_dwordx4 v[4:7], v[228:229], off offset:2048
	s_nop 0
	global_load_dwordx4 v[0:3], v[228:229], off offset:3072
	v_ashrrev_i32_e32 v33, 31, v32
	v_lshl_add_u64 v[32:33], v[32:33], 2, s[40:41]
	v_lshlrev_b64 v[82:83], 16, v[34:35]
	v_lshl_add_u64 v[82:83], v[32:33], 0, v[82:83]
	global_load_dword v69, v[82:83], off
	v_or_b32_e32 v82, 1, v34
	v_ashrrev_i32_e32 v83, 31, v82
	v_lshlrev_b64 v[82:83], 16, v[82:83]
	v_lshl_add_u64 v[82:83], v[32:33], 0, v[82:83]
	global_load_dword v81, v[82:83], off
	v_or_b32_e32 v82, 2, v34
	v_or_b32_e32 v84, 3, v34
	v_ashrrev_i32_e32 v83, 31, v82
	v_ashrrev_i32_e32 v85, 31, v84
	v_lshlrev_b64 v[82:83], 16, v[82:83]
	v_lshlrev_b64 v[84:85], 16, v[84:85]
	v_lshl_add_u64 v[82:83], v[32:33], 0, v[82:83]
	v_lshl_add_u64 v[84:85], v[32:33], 0, v[84:85]
	global_load_dword v82, v[82:83], off
	v_or_b32_e32 v86, 5, v34
	global_load_dword v83, v[84:85], off
	v_or_b32_e32 v84, 4, v34
	v_ashrrev_i32_e32 v85, 31, v84
	v_ashrrev_i32_e32 v87, 31, v86
	v_lshlrev_b64 v[84:85], 16, v[84:85]
	v_lshlrev_b64 v[86:87], 16, v[86:87]
	v_lshl_add_u64 v[84:85], v[32:33], 0, v[84:85]
	v_lshl_add_u64 v[86:87], v[32:33], 0, v[86:87]
	global_load_dword v84, v[84:85], off
	v_lshlrev_b32_e32 v91, 2, v80
	global_load_dword v85, v[86:87], off
	v_or_b32_e32 v86, 6, v34
	v_or_b32_e32 v34, 7, v34
	v_ashrrev_i32_e32 v87, 31, v86
	v_ashrrev_i32_e32 v35, 31, v34
	v_lshlrev_b64 v[86:87], 16, v[86:87]
	v_lshlrev_b64 v[34:35], 16, v[34:35]
	v_lshl_add_u64 v[86:87], v[32:33], 0, v[86:87]
	v_lshl_add_u64 v[32:33], v[32:33], 0, v[34:35]
	global_load_dword v86, v[86:87], off
	v_or_b32_e32 v97, 1, v91
	global_load_dword v87, v[32:33], off
	v_and_b32_e32 v32, -16, v90
	v_mul_u32_u24_e32 v33, 0x110, v88
	v_add3_u32 v89, 0, v32, v33
	ds_read_b128 v[32:35], v89
	ds_read_b128 v[92:95], v89 offset:64
	s_waitcnt vmcnt(15) lgkmcnt(1)
	v_mfma_f32_16x16x32_bf16 v[32:35], v[32:35], v[28:31], 0
	ds_read_b128 v[108:111], v89 offset:4416
	ds_read_b128 v[116:119], v89 offset:13120
	v_sub_u32_e32 v98, 0x7f, v97
	s_waitcnt vmcnt(14) lgkmcnt(2)
	v_mfma_f32_16x16x32_bf16 v[32:35], v[92:95], v[24:27], v[32:35]
	ds_read_b128 v[92:95], v89 offset:128
	v_or_b32_e32 v103, 2, v91
	v_sub_u32_e32 v104, 0x7f, v103
	s_waitcnt vmcnt(13) lgkmcnt(0)
	v_mfma_f32_16x16x32_bf16 v[32:35], v[92:95], v[20:23], v[32:35]
	ds_read_b128 v[92:95], v89 offset:192
	v_or_b32_e32 v105, 3, v91
	v_sub_u32_e32 v106, 0x7f, v105
	s_waitcnt vmcnt(12) lgkmcnt(0)
; #define LAS __attribute__((address_space(3)))
; __device__ __forceinline__ f32x4 mfma16(bf16x8 a, bf16x8 b, f32x4 c) { return __builtin_amdgcn_mfma_f32_16x16x32_bf16(a, b, c, 0, 0, 0); }
; __device__ __forceinline__ void topk_task(const Frame& F, int l, int tb, int h, const LAS unsigned char* kl, LAS float* tl, const LAS unsigned char* cab) {
;     ...
;         const LAS unsigned char* kbase = kl + (p * 128 + c) * KL_PITCH + rq * 16;
; #pragma unroll
;         for (int kb = 0; kb < 8; ++kb) {
;             f32x4 a = (f32x4){0.f, 0.f, 0.f, 0.f};
; #pragma unroll
;             for (int ks = 0; ks < 4; ++ks) a = mfma16(*(const LAS bf16x8*)(kbase + kb * 16 * KL_PITCH + ks * 64), Qf[ks], a);
; #pragma unroll
;             for (int e = 0; e < 4; ++e) v[kb * 4 + e] = embed_idx<127u>(a[e], (unsigned)(kb * 16 + rq * 4 + e));
	v_mfma_f32_16x16x32_bf16 v[32:35], v[92:95], v[16:19], v[32:35]
	v_sub_u32_e32 v94, 0x7f, v91
	ds_read_b128 v[124:127], v89 offset:17472
	ds_read_b128 v[132:135], v89 offset:21824
	s_nop 4
	v_cmp_gt_i32_e32 vcc, 0, v32
	ds_read_b128 v[164:167], v89 offset:26176
	v_sub_u32_e32 v93, 0x6f, v91
	v_cndmask_b32_e32 v92, v94, v91, vcc
	v_cmp_gt_i32_e32 vcc, 0, v33
	v_and_or_b32 v143, v32, s79, v92
	v_add_u32_e32 v92, 16, v91
	v_cndmask_b32_e32 v32, v98, v97, vcc
	v_cmp_gt_i32_e32 vcc, 0, v34
	v_and_or_b32 v144, v33, s79, v32
	v_sub_u32_e32 v96, 0x6e, v91
	v_cndmask_b32_e32 v32, v104, v103, vcc
	v_cmp_gt_i32_e32 vcc, 0, v35
	v_and_or_b32 v145, v34, s79, v32
	v_add_u32_e32 v99, 18, v91
	v_cndmask_b32_e32 v32, v106, v105, vcc
	v_and_or_b32 v146, v35, s79, v32
	ds_read_b128 v[32:35], v89 offset:4352
	s_waitcnt lgkmcnt(0)
	v_mfma_f32_16x16x32_bf16 v[32:35], v[32:35], v[28:31], 0
	v_sub_u32_e32 v100, 0x6d, v91
	v_add_u32_e32 v101, 19, v91
	v_sub_u32_e32 v102, 0x6c, v91
	v_mfma_f32_16x16x32_bf16 v[32:35], v[108:111], v[24:27], v[32:35]
	ds_read_b128 v[108:111], v89 offset:4480
	v_sub_u32_e32 v140, 29, v91
	v_sub_u32_e32 v142, 28, v91
	s_waitcnt lgkmcnt(0)
	v_mfma_f32_16x16x32_bf16 v[32:35], v[108:111], v[20:23], v[32:35]
	ds_read_b128 v[108:111], v89 offset:4544
	v_cmp_gt_u32_e64 s[34:35], 16, v90
	s_waitcnt lgkmcnt(0)
	v_mfma_f32_16x16x32_bf16 v[32:35], v[108:111], v[16:19], v[32:35]
	ds_read_b128 v[108:111], v89 offset:8768
	s_nop 6
	v_cmp_gt_i32_e32 vcc, 0, v32
	s_nop 1
	v_cndmask_b32_e32 v95, v93, v92, vcc
	v_and_or_b32 v147, v32, s79, v95
	v_add_u32_e32 v95, 17, v91
	v_cmp_gt_i32_e32 vcc, 0, v33
	s_nop 1
	v_cndmask_b32_e32 v32, v96, v95, vcc
	v_cmp_gt_i32_e32 vcc, 0, v34
	v_and_or_b32 v148, v33, s79, v32
	s_nop 0
	v_cndmask_b32_e32 v32, v100, v99, vcc
	v_cmp_gt_i32_e32 vcc, 0, v35
	v_and_or_b32 v149, v34, s79, v32
	s_nop 0
	v_cndmask_b32_e32 v32, v102, v101, vcc
	v_and_or_b32 v150, v35, s79, v32
	ds_read_b128 v[32:35], v89 offset:8704
	s_waitcnt lgkmcnt(0)
	v_mfma_f32_16x16x32_bf16 v[32:35], v[32:35], v[28:31], 0
	v_mfma_f32_16x16x32_bf16 v[32:35], v[108:111], v[24:27], v[32:35]
	ds_read_b128 v[108:111], v89 offset:8832
	s_waitcnt lgkmcnt(0)
	v_mfma_f32_16x16x32_bf16 v[32:35], v[108:111], v[20:23], v[32:35]
	ds_read_b128 v[108:111], v89 offset:8896
	s_waitcnt lgkmcnt(0)
	v_mfma_f32_16x16x32_bf16 v[108:111], v[108:111], v[16:19], v[32:35]
	s_nop 4
	v_add_u32_e32 v32, 32, v91
	v_sub_u32_e32 v33, 0x5f, v91
	v_sub_u32_e32 v35, 0x5e, v91
	v_cmp_gt_i32_e32 vcc, 0, v108
	s_nop 1
	v_cndmask_b32_e32 v34, v33, v32, vcc
	v_and_or_b32 v151, v108, s79, v34
	v_add_u32_e32 v34, 33, v91
	v_cmp_gt_i32_e32 vcc, 0, v109
	v_sub_u32_e32 v108, 0x5d, v91
	s_nop 0
	v_cndmask_b32_e32 v107, v35, v34, vcc
	v_and_or_b32 v152, v109, s79, v107
	v_add_u32_e32 v107, 34, v91
	v_cmp_gt_i32_e32 vcc, 0, v110
	s_nop 1
	v_cndmask_b32_e32 v109, v108, v107, vcc
	v_and_or_b32 v153, v110, s79, v109
	v_add_u32_e32 v109, 35, v91
	v_sub_u32_e32 v110, 0x5c, v91
	v_cmp_gt_i32_e32 vcc, 0, v111
	s_nop 1
	v_cndmask_b32_e32 v112, v110, v109, vcc
	v_and_or_b32 v154, v111, s79, v112
	ds_read_b128 v[112:115], v89 offset:13056
	s_waitcnt lgkmcnt(0)
	v_mfma_f32_16x16x32_bf16 v[112:115], v[112:115], v[28:31], 0
	v_add_u32_e32 v111, 48, v91
	v_mfma_f32_16x16x32_bf16 v[112:115], v[116:119], v[24:27], v[112:115]
	ds_read_b128 v[116:119], v89 offset:13184
	s_waitcnt lgkmcnt(0)
	v_mfma_f32_16x16x32_bf16 v[112:115], v[116:119], v[20:23], v[112:115]
	ds_read_b128 v[116:119], v89 offset:13248
	s_waitcnt lgkmcnt(0)
	v_mfma_f32_16x16x32_bf16 v[116:119], v[116:119], v[16:19], v[112:115]
	s_nop 4
	v_sub_u32_e32 v112, 0x4f, v91
	v_sub_u32_e32 v114, 0x4e, v91
	s_nop 0
	v_cmp_gt_i32_e32 vcc, 0, v116
	s_nop 1
	v_cndmask_b32_e32 v113, v112, v111, vcc
	v_and_or_b32 v155, v116, s79, v113
	v_add_u32_e32 v113, 49, v91
	v_cmp_gt_i32_e32 vcc, 0, v117
	v_sub_u32_e32 v116, 0x4d, v91
	s_nop 0
	v_cndmask_b32_e32 v115, v114, v113, vcc
	v_and_or_b32 v156, v117, s79, v115
	v_add_u32_e32 v115, 50, v91
	v_cmp_gt_i32_e32 vcc, 0, v118
	s_nop 1
	v_cndmask_b32_e32 v117, v116, v115, vcc
	v_and_or_b32 v157, v118, s79, v117
	v_add_u32_e32 v117, 51, v91
	v_sub_u32_e32 v118, 0x4c, v91
	v_cmp_gt_i32_e32 vcc, 0, v119
	s_nop 1
	v_cndmask_b32_e32 v120, v118, v117, vcc
	v_and_or_b32 v158, v119, s79, v120
	ds_read_b128 v[120:123], v89 offset:17408
	s_waitcnt lgkmcnt(0)
	v_mfma_f32_16x16x32_bf16 v[120:123], v[120:123], v[28:31], 0
	v_add_u32_e32 v119, 64, v91
	v_mfma_f32_16x16x32_bf16 v[120:123], v[124:127], v[24:27], v[120:123]
	ds_read_b128 v[124:127], v89 offset:17536
	s_waitcnt lgkmcnt(0)
	v_mfma_f32_16x16x32_bf16 v[120:123], v[124:127], v[20:23], v[120:123]
	ds_read_b128 v[124:127], v89 offset:17600
	s_waitcnt lgkmcnt(0)
	v_mfma_f32_16x16x32_bf16 v[124:127], v[124:127], v[16:19], v[120:123]
	s_nop 4
	v_sub_u32_e32 v120, 63, v91
	v_sub_u32_e32 v122, 62, v91
	s_nop 0
	v_cmp_gt_i32_e32 vcc, 0, v124
	s_nop 1
	v_cndmask_b32_e32 v121, v120, v119, vcc
	v_and_or_b32 v159, v124, s79, v121
	v_add_u32_e32 v121, 0x41, v91
	v_cmp_gt_i32_e32 vcc, 0, v125
	v_sub_u32_e32 v124, 61, v91
	s_nop 0
	v_cndmask_b32_e32 v123, v122, v121, vcc
	v_and_or_b32 v160, v125, s79, v123
	v_add_u32_e32 v123, 0x42, v91
	v_cmp_gt_i32_e32 vcc, 0, v126
	s_nop 1
	v_cndmask_b32_e32 v125, v124, v123, vcc
	v_and_or_b32 v161, v126, s79, v125
	v_add_u32_e32 v125, 0x43, v91
	v_sub_u32_e32 v126, 60, v91
	v_cmp_gt_i32_e32 vcc, 0, v127
	s_nop 1
	v_cndmask_b32_e32 v128, v126, v125, vcc
	v_and_or_b32 v162, v127, s79, v128
	ds_read_b128 v[128:131], v89 offset:21760
	s_waitcnt lgkmcnt(0)
; #define LAS __attribute__((address_space(3)))
; __device__ __forceinline__ f32x4 mfma16(bf16x8 a, bf16x8 b, f32x4 c) { return __builtin_amdgcn_mfma_f32_16x16x32_bf16(a, b, c, 0, 0, 0); }
; template <int N> __device__ __forceinline__ void sortdesc(float (&v)[N]) {
; #pragma unroll
;     for (int k = 2; k <= N; k <<= 1)
; #pragma unroll
;         for (int j = k >> 1; j > 0; j >>= 1)
; __device__ __forceinline__ void topk_task(const Frame& F, int l, int tb, int h, const LAS unsigned char* kl, LAS float* tl, const LAS unsigned char* cab) {
;     ...
; #pragma unroll
;         for (int kb = 0; kb < 8; ++kb) {
;             f32x4 a = (f32x4){0.f, 0.f, 0.f, 0.f};
; #pragma unroll
;             for (int ks = 0; ks < 4; ++ks) a = mfma16(*(const LAS bf16x8*)(kbase + kb * 16 * KL_PITCH + ks * 64), Qf[ks], a);
; #pragma unroll
;             for (int e = 0; e < 4; ++e) v[kb * 4 + e] = embed_idx<127u>(a[e], (unsigned)(kb * 16 + rq * 4 + e));
;         }
;         sortdesc<32>(v);
	v_mfma_f32_16x16x32_bf16 v[128:131], v[128:131], v[28:31], 0
	v_add_u32_e32 v127, 0x50, v91
	v_mfma_f32_16x16x32_bf16 v[128:131], v[132:135], v[24:27], v[128:131]
	ds_read_b128 v[132:135], v89 offset:21888
	s_waitcnt lgkmcnt(0)
	v_mfma_f32_16x16x32_bf16 v[128:131], v[132:135], v[20:23], v[128:131]
	ds_read_b128 v[132:135], v89 offset:21952
	s_waitcnt lgkmcnt(0)
	v_mfma_f32_16x16x32_bf16 v[132:135], v[132:135], v[16:19], v[128:131]
	s_nop 4
	v_sub_u32_e32 v128, 47, v91
	v_sub_u32_e32 v130, 46, v91
	s_nop 0
	v_cmp_gt_i32_e32 vcc, 0, v132
	s_nop 1
	v_cndmask_b32_e32 v129, v128, v127, vcc
	v_and_or_b32 v163, v132, s79, v129
	v_add_u32_e32 v129, 0x51, v91
	v_cmp_gt_i32_e32 vcc, 0, v133
	v_sub_u32_e32 v132, 45, v91
	s_nop 0
	v_cndmask_b32_e32 v131, v130, v129, vcc
	v_and_or_b32 v168, v133, s79, v131
	v_add_u32_e32 v131, 0x52, v91
	v_cmp_gt_i32_e32 vcc, 0, v134
	s_nop 1
	v_cndmask_b32_e32 v133, v132, v131, vcc
	v_and_or_b32 v169, v134, s79, v133
	v_add_u32_e32 v133, 0x53, v91
	v_sub_u32_e32 v134, 44, v91
	v_cmp_gt_i32_e32 vcc, 0, v135
	s_nop 1
	v_cndmask_b32_e32 v136, v134, v133, vcc
	v_and_or_b32 v170, v135, s79, v136
	ds_read_b128 v[136:139], v89 offset:26112
	s_waitcnt lgkmcnt(0)
	v_mfma_f32_16x16x32_bf16 v[136:139], v[136:139], v[28:31], 0
	v_add_u32_e32 v135, 0x60, v91
	v_mfma_f32_16x16x32_bf16 v[136:139], v[164:167], v[24:27], v[136:139]
	ds_read_b128 v[164:167], v89 offset:26240
	s_waitcnt lgkmcnt(0)
	v_mfma_f32_16x16x32_bf16 v[136:139], v[164:167], v[20:23], v[136:139]
	ds_read_b128 v[164:167], v89 offset:26304
	s_waitcnt lgkmcnt(0)
	v_mfma_f32_16x16x32_bf16 v[164:167], v[164:167], v[16:19], v[136:139]
	s_nop 4
	v_sub_u32_e32 v136, 31, v91
	v_sub_u32_e32 v138, 30, v91
	s_nop 0
	v_cmp_gt_i32_e32 vcc, 0, v164
	s_nop 1
	v_cndmask_b32_e32 v137, v136, v135, vcc
	v_and_or_b32 v171, v164, s79, v137
	v_add_u32_e32 v137, 0x61, v91
	v_cmp_gt_i32_e32 vcc, 0, v165
	s_nop 1
	v_cndmask_b32_e32 v139, v138, v137, vcc
	v_and_or_b32 v172, v165, s79, v139
	v_add_u32_e32 v139, 0x62, v91
	v_cmp_gt_i32_e32 vcc, 0, v166
	s_nop 1
	v_cndmask_b32_e32 v141, v140, v139, vcc
	v_and_or_b32 v173, v166, s79, v141
	v_add_u32_e32 v141, 0x63, v91
	v_cmp_gt_i32_e32 vcc, 0, v167
	s_nop 1
	v_cndmask_b32_e32 v164, v142, v141, vcc
	v_and_or_b32 v174, v167, s79, v164
	ds_read_b128 v[164:167], v89 offset:30464
	s_waitcnt lgkmcnt(0)
	v_mfma_f32_16x16x32_bf16 v[28:31], v[164:167], v[28:31], 0
	ds_read_b128 v[164:167], v89 offset:30528
	s_waitcnt lgkmcnt(0)
	v_mfma_f32_16x16x32_bf16 v[24:27], v[164:167], v[24:27], v[28:31]
	s_nop 4
	ds_read_b128 v[28:31], v89 offset:30592
	v_max_f32_e32 v164, v171, v171
	v_max_f32_e32 v166, v173, v173
	s_waitcnt lgkmcnt(0)
	v_mfma_f32_16x16x32_bf16 v[20:23], v[28:31], v[20:23], v[24:27]
	s_nop 2
	ds_read_b128 v[24:27], v89 offset:30656
	v_max_f32_e32 v29, v143, v143
	v_max_f32_e32 v31, v145, v145
	s_waitcnt lgkmcnt(0)
	v_mfma_f32_16x16x32_bf16 v[22:25], v[24:27], v[16:19], v[20:23]
	v_add_u32_e32 v17, 0x70, v91
	v_sub_u32_e32 v18, 15, v91
	v_add_u32_e32 v19, 0x71, v91
	s_nop 4
	v_cmp_gt_i32_e32 vcc, 0, v22
	v_sub_u32_e32 v20, 14, v91
	s_nop 0
	v_cndmask_b32_e32 v16, v18, v17, vcc
	v_cmp_gt_i32_e32 vcc, 0, v23
	v_and_or_b32 v16, v22, s79, v16
	v_sub_u32_e32 v22, 13, v91
	v_cndmask_b32_e32 v21, v20, v19, vcc
	v_and_or_b32 v26, v23, s79, v21
	v_add_u32_e32 v21, 0x72, v91
	v_cmp_gt_i32_e32 vcc, 0, v24
	v_max_f32_e32 v26, v26, v26
	v_max_f32_e32 v16, v16, v16
	v_cndmask_b32_e32 v23, v22, v21, vcc
	v_and_or_b32 v27, v24, s79, v23
	v_add_u32_e32 v23, 0x73, v91
	v_sub_u32_e32 v24, 12, v91
	v_cmp_gt_i32_e32 vcc, 0, v25
	s_nop 1
	v_cndmask_b32_e32 v28, v24, v23, vcc
	v_and_or_b32 v25, v25, s79, v28
	v_max_f32_e32 v28, v144, v144
	v_max_f32_e32 v30, v29, v28
	v_min_f32_e32 v28, v29, v28
	v_max_f32_e32 v29, v146, v146
	v_max_f32_e32 v143, v31, v29
	v_min_f32_e32 v29, v31, v29
	v_max_f32_e32 v31, v148, v148
	v_max_f32_e32 v144, v147, v147
	v_max_f32_e32 v145, v144, v31
	v_min_f32_e32 v31, v144, v31
	v_max_f32_e32 v144, v150, v150
	v_max_f32_e32 v146, v149, v149
	v_max_f32_e32 v147, v146, v144
	v_min_f32_e32 v144, v146, v144
	v_max_f32_e32 v146, v152, v152
	v_max_f32_e32 v148, v151, v151
	v_max_f32_e32 v149, v148, v146
	v_min_f32_e32 v146, v148, v146
	v_max_f32_e32 v148, v154, v154
	v_max_f32_e32 v150, v153, v153
	v_max_f32_e32 v151, v150, v148
	v_min_f32_e32 v148, v150, v148
	v_max_f32_e32 v150, v156, v156
	v_max_f32_e32 v152, v155, v155
	v_max_f32_e32 v153, v152, v150
	v_min_f32_e32 v150, v152, v150
	v_max_f32_e32 v152, v158, v158
	v_max_f32_e32 v154, v157, v157
	v_max_f32_e32 v155, v154, v152
	v_min_f32_e32 v152, v154, v152
	v_max_f32_e32 v154, v160, v160
	v_max_f32_e32 v156, v159, v159
	v_max_f32_e32 v157, v156, v154
	v_min_f32_e32 v154, v156, v154
	v_max_f32_e32 v156, v162, v162
	v_max_f32_e32 v158, v161, v161
	v_max_f32_e32 v159, v158, v156
	v_min_f32_e32 v156, v158, v156
	v_max_f32_e32 v158, v168, v168
	v_max_f32_e32 v160, v163, v163
	v_max_f32_e32 v161, v160, v158
	v_min_f32_e32 v158, v160, v158
	v_max_f32_e32 v160, v170, v170
	v_max_f32_e32 v162, v169, v169
	v_max_f32_e32 v163, v162, v160
	v_min_f32_e32 v160, v162, v160
	v_max_f32_e32 v162, v172, v172
	v_max_f32_e32 v165, v164, v162
	v_min_f32_e32 v162, v164, v162
	v_max_f32_e32 v164, v174, v174
	v_max_f32_e32 v167, v166, v164
	v_min_f32_e32 v164, v166, v164
	v_max_f32_e32 v166, v16, v26
	v_min_f32_e32 v16, v16, v26
	v_max_f32_e32 v25, v25, v25
	v_max_f32_e32 v26, v27, v27
	v_max_f32_e32 v27, v26, v25
	v_min_f32_e32 v25, v26, v25
	v_max_f32_e32 v26, v30, v29
	v_min_f32_e32 v29, v30, v29
	v_max_f32_e32 v30, v28, v143
	v_min_f32_e32 v28, v28, v143
	v_max_f32_e32 v143, v145, v144
	v_min_f32_e32 v144, v145, v144
; template <int N> __device__ __forceinline__ void sortdesc(float (&v)[N]) {
; #pragma unroll
;     for (int k = 2; k <= N; k <<= 1)
; #pragma unroll
;         for (int j = k >> 1; j > 0; j >>= 1)
; #pragma unroll
;             for (int i = 0; i < N; ++i) { const int p = i ^ j;
;                 if (p > i) { const bool desc = ((i & k) == 0); const float a = v[i], b = v[p], hi = fmaxf(a, b), lo = fminf(a, b); v[i] = desc ? hi : lo; v[p] = desc ? lo : hi; } }
; }
	v_max_f32_e32 v145, v31, v147
	v_min_f32_e32 v31, v31, v147
	v_max_f32_e32 v147, v149, v148
	v_min_f32_e32 v148, v149, v148
	v_max_f32_e32 v149, v146, v151
	v_min_f32_e32 v146, v146, v151
	v_max_f32_e32 v151, v153, v152
	v_min_f32_e32 v152, v153, v152
	v_max_f32_e32 v153, v150, v155
	v_min_f32_e32 v150, v150, v155
	v_max_f32_e32 v155, v157, v156
	v_min_f32_e32 v156, v157, v156
	v_max_f32_e32 v157, v154, v159
	v_min_f32_e32 v154, v154, v159
	v_max_f32_e32 v159, v161, v160
	v_min_f32_e32 v160, v161, v160
	v_max_f32_e32 v161, v158, v163
	v_min_f32_e32 v158, v158, v163
	v_max_f32_e32 v163, v165, v164
	v_min_f32_e32 v164, v165, v164
	v_max_f32_e32 v165, v162, v167
	v_min_f32_e32 v162, v162, v167
	v_max_f32_e32 v167, v166, v25
	v_min_f32_e32 v25, v166, v25
	v_max_f32_e32 v166, v16, v27
	v_min_f32_e32 v16, v16, v27
	v_max_f32_e32 v27, v26, v30
	v_min_f32_e32 v26, v26, v30
	v_max_f32_e32 v30, v29, v28
	v_min_f32_e32 v28, v29, v28
	v_max_f32_e32 v29, v144, v31
	v_min_f32_e32 v31, v144, v31
	v_max_f32_e32 v144, v143, v145
	v_min_f32_e32 v143, v143, v145
	v_max_f32_e32 v145, v147, v149
	v_min_f32_e32 v147, v147, v149
	v_max_f32_e32 v149, v148, v146
	v_min_f32_e32 v146, v148, v146
	v_max_f32_e32 v148, v152, v150
	v_min_f32_e32 v150, v152, v150
	v_max_f32_e32 v152, v151, v153
	v_min_f32_e32 v151, v151, v153
	v_max_f32_e32 v153, v155, v157
	v_min_f32_e32 v155, v155, v157
	v_max_f32_e32 v157, v156, v154
	v_min_f32_e32 v154, v156, v154
	v_max_f32_e32 v156, v160, v158
	v_min_f32_e32 v158, v160, v158
	v_max_f32_e32 v160, v159, v161
	v_min_f32_e32 v159, v159, v161
	v_max_f32_e32 v161, v163, v165
	v_min_f32_e32 v163, v163, v165
	v_max_f32_e32 v165, v164, v162
	v_min_f32_e32 v162, v164, v162
	v_max_f32_e32 v164, v25, v16
	v_min_f32_e32 v16, v25, v16
	v_max_f32_e32 v25, v167, v166
	v_min_f32_e32 v166, v167, v166
	v_max_f32_e32 v167, v27, v31
	v_min_f32_e32 v27, v27, v31
	v_max_f32_e32 v31, v26, v29
	v_min_f32_e32 v26, v26, v29
	v_max_f32_e32 v29, v30, v143
	v_min_f32_e32 v30, v30, v143
	v_max_f32_e32 v143, v28, v144
	v_min_f32_e32 v28, v28, v144
	v_max_f32_e32 v144, v145, v150
	v_min_f32_e32 v145, v145, v150
	v_max_f32_e32 v150, v147, v148
	v_min_f32_e32 v147, v147, v148
	v_max_f32_e32 v148, v149, v151
	v_min_f32_e32 v149, v149, v151
	v_max_f32_e32 v151, v146, v152
	v_min_f32_e32 v146, v146, v152
	v_max_f32_e32 v152, v153, v158
	v_min_f32_e32 v153, v153, v158
	v_max_f32_e32 v158, v155, v156
	v_min_f32_e32 v155, v155, v156
	v_max_f32_e32 v156, v157, v159
	v_min_f32_e32 v157, v157, v159
	v_max_f32_e32 v159, v154, v160
	v_min_f32_e32 v154, v154, v160
	v_max_f32_e32 v160, v161, v16
	v_min_f32_e32 v16, v161, v16
	v_max_f32_e32 v161, v163, v164
	v_min_f32_e32 v163, v163, v164
	v_max_f32_e32 v164, v165, v166
	v_min_f32_e32 v165, v165, v166
	v_max_f32_e32 v166, v162, v25
	v_min_f32_e32 v25, v162, v25
	v_max_f32_e32 v162, v167, v29
	v_min_f32_e32 v29, v167, v29
	v_max_f32_e32 v167, v31, v143
	v_min_f32_e32 v31, v31, v143
	v_max_f32_e32 v143, v27, v30
	v_min_f32_e32 v27, v27, v30
	v_max_f32_e32 v30, v26, v28
	v_min_f32_e32 v26, v26, v28
	v_max_f32_e32 v28, v145, v149
	v_min_f32_e32 v145, v145, v149
	v_max_f32_e32 v149, v147, v146
	v_min_f32_e32 v146, v147, v146
	v_max_f32_e32 v147, v144, v148
	v_min_f32_e32 v144, v144, v148
	v_max_f32_e32 v148, v150, v151
	v_min_f32_e32 v150, v150, v151
	v_max_f32_e32 v151, v152, v156
	v_min_f32_e32 v152, v152, v156
	v_max_f32_e32 v156, v158, v159
	v_min_f32_e32 v158, v158, v159
	v_max_f32_e32 v159, v153, v157
	v_min_f32_e32 v153, v153, v157
	v_max_f32_e32 v157, v155, v154
	v_min_f32_e32 v154, v155, v154
	v_max_f32_e32 v155, v16, v165
	v_min_f32_e32 v16, v16, v165
	v_max_f32_e32 v165, v163, v25
	v_min_f32_e32 v25, v163, v25
	v_max_f32_e32 v163, v160, v164
	v_min_f32_e32 v160, v160, v164
	v_max_f32_e32 v164, v161, v166
	v_min_f32_e32 v161, v161, v166
	v_max_f32_e32 v166, v162, v167
	v_min_f32_e32 v162, v162, v167
	v_max_f32_e32 v167, v29, v31
	v_min_f32_e32 v29, v29, v31
	v_max_f32_e32 v31, v143, v30
	v_min_f32_e32 v30, v143, v30
	v_max_f32_e32 v143, v27, v26
	v_min_f32_e32 v26, v27, v26
	v_max_f32_e32 v27, v145, v146
	v_min_f32_e32 v145, v145, v146
	v_max_f32_e32 v146, v28, v149
	v_min_f32_e32 v28, v28, v149
	v_max_f32_e32 v149, v144, v150
	v_min_f32_e32 v144, v144, v150
	v_max_f32_e32 v150, v147, v148
	v_min_f32_e32 v147, v147, v148
	v_max_f32_e32 v148, v151, v156
	v_min_f32_e32 v151, v151, v156
	v_max_f32_e32 v156, v152, v158
	v_min_f32_e32 v152, v152, v158
	v_max_f32_e32 v158, v159, v157
	v_min_f32_e32 v157, v159, v157
	v_max_f32_e32 v159, v153, v154
	v_min_f32_e32 v153, v153, v154
	v_max_f32_e32 v154, v16, v25
	v_min_f32_e32 v16, v16, v25
	v_max_f32_e32 v25, v155, v165
	v_min_f32_e32 v155, v155, v165
	v_max_f32_e32 v165, v160, v161
	v_min_f32_e32 v160, v160, v161
	v_max_f32_e32 v161, v163, v164
	v_min_f32_e32 v163, v163, v164
	v_max_f32_e32 v164, v166, v145
	v_min_f32_e32 v145, v166, v145
	v_max_f32_e32 v166, v162, v27
	v_min_f32_e32 v27, v162, v27
	v_max_f32_e32 v162, v167, v28
	v_min_f32_e32 v28, v167, v28
	v_max_f32_e32 v167, v29, v146
	v_min_f32_e32 v29, v29, v146
	v_max_f32_e32 v146, v31, v144
	v_min_f32_e32 v31, v31, v144
	v_max_f32_e32 v144, v30, v149
	v_min_f32_e32 v30, v30, v149
	v_max_f32_e32 v149, v143, v147
	v_min_f32_e32 v143, v143, v147
	v_max_f32_e32 v147, v26, v150
	v_min_f32_e32 v26, v26, v150
	v_max_f32_e32 v150, v148, v16
	v_min_f32_e32 v16, v148, v16
	v_max_f32_e32 v148, v151, v154
	v_min_f32_e32 v151, v151, v154
	v_max_f32_e32 v154, v156, v155
	v_min_f32_e32 v155, v156, v155
	v_max_f32_e32 v156, v152, v25
	v_min_f32_e32 v25, v152, v25
	v_max_f32_e32 v152, v158, v160
	v_min_f32_e32 v158, v158, v160
; template <int N> __device__ __forceinline__ void sortdesc(float (&v)[N]) {
; #pragma unroll
;     for (int k = 2; k <= N; k <<= 1)
; #pragma unroll
;         for (int j = k >> 1; j > 0; j >>= 1)
; #pragma unroll
;             for (int i = 0; i < N; ++i) { const int p = i ^ j;
;                 if (p > i) { const bool desc = ((i & k) == 0); const float a = v[i], b = v[p], hi = fmaxf(a, b), lo = fminf(a, b); v[i] = desc ? hi : lo; v[p] = desc ? lo : hi; } }
; }
; __device__ __forceinline__ void merge16(float (&v)[16]) {
; #pragma unroll
;     for (int j = 8; j > 0; j >>= 1)
; #pragma unroll
;         for (int i = 0; i < 16; ++i) { const int p = i ^ j; if (p > i) { const float a = v[i], b = v[p]; v[i] = fmaxf(a, b); v[p] = fminf(a, b); } }
; }
; __device__ __forceinline__ void top16_of_group(float (&a)[16]) {
; #pragma unroll
;     for (int sh = 16; sh <= 32; sh <<= 1) {
;         float cc[16];
; #pragma unroll
;         for (int i = 0; i < 16; ++i) cc[i] = fmaxf(a[i], __shfl_xor(a[15 - i], sh));
;         merge16(cc);
; #pragma unroll
;         for (int i = 0; i < 16; ++i) a[i] = cc[i];
;     }
; }
	v_max_f32_e32 v160, v157, v165
	v_min_f32_e32 v157, v157, v165
	v_max_f32_e32 v165, v159, v163
	v_min_f32_e32 v159, v159, v163
	v_max_f32_e32 v163, v153, v161
	v_min_f32_e32 v153, v153, v161
	v_max_f32_e32 v161, v164, v146
	v_min_f32_e32 v146, v164, v146
	v_max_f32_e32 v164, v166, v144
	v_min_f32_e32 v144, v166, v144
	v_max_f32_e32 v166, v162, v149
	v_min_f32_e32 v149, v162, v149
	v_max_f32_e32 v162, v167, v147
	v_min_f32_e32 v147, v167, v147
	v_max_f32_e32 v167, v145, v31
	v_min_f32_e32 v31, v145, v31
	v_max_f32_e32 v145, v27, v30
	v_min_f32_e32 v27, v27, v30
	v_max_f32_e32 v30, v28, v143
	v_min_f32_e32 v28, v28, v143
	v_max_f32_e32 v143, v29, v26
	v_min_f32_e32 v26, v29, v26
	v_max_f32_e32 v29, v16, v158
	v_min_f32_e32 v16, v16, v158
	v_max_f32_e32 v158, v151, v157
	v_min_f32_e32 v151, v151, v157
	v_max_f32_e32 v157, v155, v159
	v_min_f32_e32 v155, v155, v159
	v_max_f32_e32 v159, v25, v153
	v_min_f32_e32 v25, v25, v153
	v_max_f32_e32 v153, v150, v152
	v_min_f32_e32 v150, v150, v152
	v_max_f32_e32 v152, v148, v160
	v_min_f32_e32 v148, v148, v160
	v_max_f32_e32 v160, v154, v165
	v_min_f32_e32 v154, v154, v165
	v_max_f32_e32 v165, v156, v163
	v_min_f32_e32 v156, v156, v163
	v_max_f32_e32 v163, v161, v166
	v_min_f32_e32 v161, v161, v166
	v_max_f32_e32 v166, v164, v162
	v_min_f32_e32 v162, v164, v162
	v_max_f32_e32 v164, v146, v149
	v_min_f32_e32 v146, v146, v149
	v_max_f32_e32 v149, v144, v147
	v_min_f32_e32 v144, v144, v147
	v_max_f32_e32 v147, v167, v30
	v_min_f32_e32 v30, v167, v30
	v_max_f32_e32 v167, v145, v143
	v_min_f32_e32 v143, v145, v143
	v_max_f32_e32 v145, v31, v28
	v_min_f32_e32 v28, v31, v28
	v_max_f32_e32 v31, v27, v26
	v_min_f32_e32 v26, v27, v26
	v_max_f32_e32 v27, v16, v155
	v_min_f32_e32 v16, v16, v155
	v_max_f32_e32 v155, v151, v25
	v_min_f32_e32 v25, v151, v25
	v_max_f32_e32 v151, v29, v157
	v_min_f32_e32 v29, v29, v157
	v_max_f32_e32 v157, v158, v159
	v_min_f32_e32 v158, v158, v159
	v_max_f32_e32 v159, v150, v154
	v_min_f32_e32 v150, v150, v154
	v_max_f32_e32 v154, v148, v156
	v_min_f32_e32 v148, v148, v156
	v_max_f32_e32 v156, v153, v160
	v_min_f32_e32 v153, v153, v160
	v_max_f32_e32 v160, v152, v165
	v_min_f32_e32 v152, v152, v165
	v_min_f32_e32 v165, v163, v166
	v_min_f32_e32 v168, v161, v162
	v_min_f32_e32 v169, v164, v149
	v_min_f32_e32 v170, v146, v144
	v_min_f32_e32 v171, v147, v167
	v_min_f32_e32 v172, v30, v143
	v_min_f32_e32 v173, v145, v31
	v_min_f32_e32 v174, v28, v26
	v_min_f32_e32 v175, v16, v25
	v_min_f32_e32 v176, v27, v155
	v_min_f32_e32 v177, v29, v158
	v_min_f32_e32 v178, v151, v157
	v_min_f32_e32 v179, v150, v148
	v_min_f32_e32 v180, v159, v154
	v_min_f32_e32 v181, v153, v152
	v_min_f32_e32 v182, v156, v160
	v_max3_f32 v163, v163, v166, v175
	v_max3_f32 v16, v165, v16, v25
	v_max3_f32 v25, v161, v162, v176
	v_max3_f32 v27, v168, v27, v155
	v_max3_f32 v149, v164, v149, v177
	v_max3_f32 v29, v169, v29, v158
	v_max3_f32 v144, v146, v144, v178
	v_max3_f32 v146, v170, v151, v157
	v_max3_f32 v147, v147, v167, v179
	v_max3_f32 v148, v171, v150, v148
	v_max3_f32 v30, v30, v143, v180
	v_max3_f32 v143, v172, v159, v154
	v_max3_f32 v31, v145, v31, v181
	v_max3_f32 v145, v173, v153, v152
	v_max3_f32 v26, v28, v26, v182
	v_max3_f32 v28, v174, v156, v160
	v_max_f32_e32 v150, v163, v147
	v_min_f32_e32 v147, v163, v147
	v_max_f32_e32 v151, v16, v148
	v_min_f32_e32 v16, v16, v148
	v_max_f32_e32 v148, v25, v30
	v_min_f32_e32 v25, v25, v30
	v_max_f32_e32 v30, v27, v143
	v_min_f32_e32 v27, v27, v143
	v_max_f32_e32 v143, v149, v31
	v_min_f32_e32 v31, v149, v31
	v_max_f32_e32 v149, v29, v145
	v_min_f32_e32 v29, v29, v145
	v_max_f32_e32 v145, v144, v26
	v_min_f32_e32 v26, v144, v26
	v_max_f32_e32 v144, v146, v28
	v_min_f32_e32 v28, v146, v28
	v_max_f32_e32 v146, v150, v143
	v_min_f32_e32 v143, v150, v143
	v_max_f32_e32 v150, v151, v149
	v_min_f32_e32 v149, v151, v149
	v_max_f32_e32 v151, v148, v145
	v_min_f32_e32 v145, v148, v145
	v_max_f32_e32 v148, v30, v144
	v_min_f32_e32 v30, v30, v144
	v_max_f32_e32 v144, v147, v31
	v_min_f32_e32 v31, v147, v31
	v_max_f32_e32 v147, v16, v29
	v_min_f32_e32 v16, v16, v29
	v_max_f32_e32 v29, v25, v26
	v_min_f32_e32 v25, v25, v26
	v_max_f32_e32 v26, v27, v28
	v_min_f32_e32 v27, v27, v28
	v_max_f32_e32 v28, v146, v151
	v_min_f32_e32 v146, v146, v151
	v_max_f32_e32 v151, v150, v148
	v_min_f32_e32 v148, v150, v148
	v_max_f32_e32 v150, v143, v145
	v_min_f32_e32 v143, v143, v145
	v_max_f32_e32 v145, v149, v30
	v_min_f32_e32 v30, v149, v30
	v_max_f32_e32 v149, v144, v29
	v_min_f32_e32 v29, v144, v29
	v_max_f32_e32 v144, v147, v26
	v_min_f32_e32 v26, v147, v26
	v_max_f32_e32 v147, v31, v25
	v_min_f32_e32 v25, v31, v25
	v_max_f32_e32 v31, v16, v27
	v_min_f32_e32 v16, v16, v27
	v_max_f32_e32 v27, v28, v151
	v_min_f32_e32 v28, v28, v151
	v_max_f32_e32 v151, v146, v148
	v_min_f32_e32 v146, v146, v148
	v_max_f32_e32 v148, v150, v145
	v_min_f32_e32 v145, v150, v145
	v_max_f32_e32 v150, v143, v30
	v_min_f32_e32 v30, v143, v30
	v_max_f32_e32 v143, v149, v144
	ds_bpermute_b32 v158, v70, v143
	v_min_f32_e32 v144, v149, v144
	v_max_f32_e32 v149, v29, v26
	ds_bpermute_b32 v156, v70, v149
	ds_bpermute_b32 v157, v70, v144
	s_waitcnt lgkmcnt(2)
	v_max_f32_e32 v158, v158, v158
	v_max_f32_e32 v158, v30, v158
	ds_bpermute_b32 v30, v70, v30
	s_waitcnt lgkmcnt(2)
	v_max_f32_e32 v156, v156, v156
	v_max_f32_e32 v156, v145, v156
	v_min_f32_e32 v26, v29, v26
	v_max_f32_e32 v29, v147, v31
	s_waitcnt lgkmcnt(0)
	v_max_f32_e32 v30, v30, v30
	v_max_f32_e32 v30, v143, v30
	ds_bpermute_b32 v143, v70, v150
	v_min_f32_e32 v31, v147, v31
	v_max_f32_e32 v147, v25, v16
	v_min_f32_e32 v16, v25, v16
	ds_bpermute_b32 v25, v70, v16
	s_waitcnt lgkmcnt(1)
; #define GAS __attribute__((address_space(1)))
; #define LAS __attribute__((address_space(3)))
; __device__ __forceinline__ void top16_of_group(float (&a)[16]) {
; #pragma unroll
;     for (int sh = 16; sh <= 32; sh <<= 1) {
;         float cc[16];
; #pragma unroll
;         for (int i = 0; i < 16; ++i) cc[i] = fmaxf(a[i], __shfl_xor(a[15 - i], sh));
;         merge16(cc);
; #pragma unroll
;         for (int i = 0; i < 16; ++i) a[i] = cc[i];
;     }
; }
; __device__ __forceinline__ void topk_task(const Frame& F, int l, int tb, int h, const LAS unsigned char* kl, LAS float* tl, const LAS unsigned char* cab) {
;     int lane = lane_id(); asm volatile("" : "+v"(lane));
;     const int c = lane & 15, rq = lane >> 4;
;     const int t0 = tb * 16;
;     const bf16* QP = (const bf16*)(F.ws + WS_QP);
;     int* EXPI = (int*)(F.ws + WS_EXP); float* GATE = (float*)(F.ws + WS_GATE);
;     const float NEG = -__builtin_inff();
;     bf16x8 Qall[2][4];
; #pragma unroll
;     for (int p = 0; p < 2; ++p)
; #pragma unroll
;         for (int ks = 0; ks < 4; ++ks) Qall[p][ks] = ld_b8(QP + (size_t)(t0 + c) * QPP + h * 256 + p * 128 + ks * 32 + rq * 8);
;     float rsp[8];
;     { const float* SS2 = (const float*)(F.ws + WS_SS2) + (t0 + c);
; #pragma unroll
;         for (int i = 0; i < 8; ++i) rsp[i] = *(const GAS float*)(SS2 + (size_t)(rq * 8 + i) * T); }
; #pragma unroll
;     for (int p = 0; p < 2; ++p) {
;         bf16x8 Qf[4];
; #pragma unroll
;         for (int ks = 0; ks < 4; ++ks) Qf[ks] = Qall[p][ks];
;         float v[32];
;         const LAS unsigned char* kbase = kl + (p * 128 + c) * KL_PITCH + rq * 16;
; #pragma unroll
;         for (int kb = 0; kb < 8; ++kb) {
;             f32x4 a = (f32x4){0.f, 0.f, 0.f, 0.f};
; #pragma unroll
;             for (int ks = 0; ks < 4; ++ks) a = mfma16(*(const LAS bf16x8*)(kbase + kb * 16 * KL_PITCH + ks * 64), Qf[ks], a);
; #pragma unroll
;             for (int e = 0; e < 4; ++e) v[kb * 4 + e] = embed_idx<127u>(a[e], (unsigned)(kb * 16 + rq * 4 + e));
;         }
;         sortdesc<32>(v);
;         float top[16];
; #pragma unroll
;         for (int i = 0; i < 16; ++i) top[i] = v[i];
;         top16_of_group(top);
;         if (rq == 0) {
; #pragma unroll
;             for (int it = 0; it < 16; ++it) tl[(p * 16 + c) * TL_STRIDE + it] = top[it];
	v_max_f32_e32 v143, v143, v143
	v_max_f32_e32 v143, v144, v143
	ds_bpermute_b32 v144, v70, v145
	ds_bpermute_b32 v145, v70, v148
	ds_bpermute_b32 v152, v70, v147
	ds_bpermute_b32 v155, v70, v26
	s_waitcnt lgkmcnt(4)
	v_max_f32_e32 v25, v25, v25
	v_max_f32_e32 v25, v27, v25
	s_waitcnt lgkmcnt(2)
	v_max_f32_e32 v145, v145, v145
	v_max_f32_e32 v26, v26, v145
	ds_bpermute_b32 v145, v70, v146
	s_waitcnt lgkmcnt(2)
	v_max_f32_e32 v152, v152, v152
	v_max_f32_e32 v152, v28, v152
	ds_bpermute_b32 v153, v70, v31
	ds_bpermute_b32 v154, v70, v29
	s_waitcnt lgkmcnt(2)
	v_max_f32_e32 v145, v145, v145
	v_max_f32_e32 v29, v29, v145
	ds_bpermute_b32 v145, v70, v151
	ds_bpermute_b32 v28, v70, v28
	ds_bpermute_b32 v27, v70, v27
	s_waitcnt lgkmcnt(4)
	v_max_f32_e32 v153, v153, v153
	s_waitcnt lgkmcnt(3)
	v_max_f32_e32 v154, v154, v154
	v_max_f32_e32 v155, v155, v155
	v_max_f32_e32 v157, v157, v157
	v_max_f32_e32 v144, v144, v144
	s_waitcnt lgkmcnt(2)
	v_max_f32_e32 v145, v145, v145
	s_waitcnt lgkmcnt(1)
	v_max_f32_e32 v28, v28, v28
	s_waitcnt lgkmcnt(0)
	v_max_f32_e32 v27, v27, v27
	v_max_f32_e32 v153, v151, v153
	v_max_f32_e32 v154, v146, v154
	v_max_f32_e32 v155, v148, v155
	v_max_f32_e32 v157, v150, v157
	v_max_f32_e32 v144, v149, v144
	v_max_f32_e32 v31, v31, v145
	v_max_f32_e32 v28, v147, v28
	v_max_f32_e32 v16, v16, v27
	v_max_f32_e32 v27, v25, v30
	v_min_f32_e32 v25, v25, v30
	v_max_f32_e32 v30, v152, v143
	v_min_f32_e32 v143, v152, v143
	v_max_f32_e32 v145, v153, v144
	v_min_f32_e32 v144, v153, v144
	v_max_f32_e32 v146, v154, v26
	v_min_f32_e32 v26, v154, v26
	v_max_f32_e32 v147, v155, v29
	v_min_f32_e32 v29, v155, v29
	v_max_f32_e32 v148, v156, v31
	v_min_f32_e32 v31, v156, v31
	v_max_f32_e32 v149, v157, v28
	v_min_f32_e32 v28, v157, v28
	v_max_f32_e32 v150, v158, v16
	v_min_f32_e32 v16, v158, v16
	v_max_f32_e32 v151, v27, v147
	v_min_f32_e32 v27, v27, v147
	v_max_f32_e32 v147, v30, v148
	v_min_f32_e32 v30, v30, v148
	v_max_f32_e32 v148, v145, v149
	v_min_f32_e32 v145, v145, v149
	v_max_f32_e32 v149, v146, v150
	v_min_f32_e32 v146, v146, v150
	v_max_f32_e32 v150, v25, v29
	v_min_f32_e32 v25, v25, v29
	v_max_f32_e32 v29, v143, v31
	v_min_f32_e32 v31, v143, v31
	v_max_f32_e32 v143, v144, v28
	v_min_f32_e32 v28, v144, v28
	v_max_f32_e32 v144, v26, v16
	v_min_f32_e32 v16, v26, v16
	v_max_f32_e32 v26, v151, v148
	v_min_f32_e32 v148, v151, v148
	v_max_f32_e32 v151, v147, v149
	v_min_f32_e32 v147, v147, v149
	v_max_f32_e32 v149, v27, v145
	v_min_f32_e32 v27, v27, v145
	v_max_f32_e32 v145, v30, v146
	v_min_f32_e32 v146, v30, v146
	v_max_f32_e32 v152, v150, v143
	v_min_f32_e32 v143, v150, v143
	v_max_f32_e32 v153, v29, v144
	v_min_f32_e32 v144, v29, v144
	v_max_f32_e32 v155, v25, v28
	v_min_f32_e32 v158, v25, v28
	v_max_f32_e32 v160, v31, v16
	v_min_f32_e32 v16, v31, v16
	v_max_f32_e32 v157, v26, v151
	v_min_f32_e32 v30, v26, v151
	v_max_f32_e32 v150, v148, v147
	v_min_f32_e32 v26, v148, v147
	v_max_f32_e32 v156, v149, v145
	v_min_f32_e32 v29, v149, v145
	v_max_f32_e32 v148, v27, v146
	v_min_f32_e32 v25, v27, v146
	v_max_f32_e32 v161, v152, v153
	v_min_f32_e32 v145, v152, v153
	v_max_f32_e32 v154, v143, v144
	v_min_f32_e32 v28, v143, v144
	v_max_f32_e32 v159, v155, v160
	v_min_f32_e32 v143, v155, v160
	v_max_f32_e32 v152, v158, v16
	v_min_f32_e32 v27, v158, v16
	ds_bpermute_b32 v165, v71, v27
	ds_bpermute_b32 v151, v71, v152
	ds_bpermute_b32 v160, v71, v143
	ds_bpermute_b32 v144, v71, v159
	ds_bpermute_b32 v164, v71, v28
	ds_bpermute_b32 v149, v71, v154
	ds_bpermute_b32 v158, v71, v145
	ds_bpermute_b32 v31, v71, v161
	ds_bpermute_b32 v167, v71, v25
	ds_bpermute_b32 v155, v71, v148
	ds_bpermute_b32 v163, v71, v29
	ds_bpermute_b32 v147, v71, v156
	ds_bpermute_b32 v166, v71, v26
	ds_bpermute_b32 v153, v71, v150
	ds_bpermute_b32 v162, v71, v30
	ds_bpermute_b32 v146, v71, v157
	v_mul_lo_u32 v16, v90, s7
	v_add_u32_e32 v16, s73, v16
	s_and_saveexec_b64 s[0:1], s[34:35]
	s_cbranch_execz .LBB0_1011
; #define GAS __attribute__((address_space(1)))
; #define LAS __attribute__((address_space(3)))
; __device__ __forceinline__ f32x4 mfma16(bf16x8 a, bf16x8 b, f32x4 c) { return __builtin_amdgcn_mfma_f32_16x16x32_bf16(a, b, c, 0, 0, 0); }
; __device__ __forceinline__ void top16_of_group(float (&a)[16]) {
;     ...
;         for (int i = 0; i < 16; ++i) cc[i] = fmaxf(a[i], __shfl_xor(a[15 - i], sh));
;         merge16(cc);
; #pragma unroll
;         for (int i = 0; i < 16; ++i) a[i] = cc[i];
;     }
; }
; __device__ __forceinline__ void topk_task(const Frame& F, int l, int tb, int h, const LAS unsigned char* kl, LAS float* tl, const LAS unsigned char* cab) {
;     int lane = lane_id(); asm volatile("" : "+v"(lane));
;     const int c = lane & 15, rq = lane >> 4;
;     const int t0 = tb * 16;
;     const bf16* QP = (const bf16*)(F.ws + WS_QP);
;     int* EXPI = (int*)(F.ws + WS_EXP); float* GATE = (float*)(F.ws + WS_GATE);
;     const float NEG = -__builtin_inff();
;     bf16x8 Qall[2][4];
; #pragma unroll
;     for (int p = 0; p < 2; ++p)
; #pragma unroll
;         for (int ks = 0; ks < 4; ++ks) Qall[p][ks] = ld_b8(QP + (size_t)(t0 + c) * QPP + h * 256 + p * 128 + ks * 32 + rq * 8);
;     float rsp[8];
;     { const float* SS2 = (const float*)(F.ws + WS_SS2) + (t0 + c);
; #pragma unroll
;         for (int i = 0; i < 8; ++i) rsp[i] = *(const GAS float*)(SS2 + (size_t)(rq * 8 + i) * T); }
; #pragma unroll
;     for (int p = 0; p < 2; ++p) {
;         bf16x8 Qf[4];
; #pragma unroll
;         for (int ks = 0; ks < 4; ++ks) Qf[ks] = Qall[p][ks];
;         float v[32];
;         const LAS unsigned char* kbase = kl + (p * 128 + c) * KL_PITCH + rq * 16;
; #pragma unroll
;         for (int kb = 0; kb < 8; ++kb) {
;             f32x4 a = (f32x4){0.f, 0.f, 0.f, 0.f};
; #pragma unroll
;             for (int ks = 0; ks < 4; ++ks) a = mfma16(*(const LAS bf16x8*)(kbase + kb * 16 * KL_PITCH + ks * 64), Qf[ks], a);
; #pragma unroll
;             for (int e = 0; e < 4; ++e) v[kb * 4 + e] = embed_idx<127u>(a[e], (unsigned)(kb * 16 + rq * 4 + e));
;         }
;         sortdesc<32>(v);
;         float top[16];
; #pragma unroll
;         for (int i = 0; i < 16; ++i) top[i] = v[i];
;         top16_of_group(top);
;         if (rq == 0) {
; #pragma unroll
;             for (int it = 0; it < 16; ++it) tl[(p * 16 + c) * TL_STRIDE + it] = top[it];
;         }
	s_waitcnt lgkmcnt(14)
	v_max_f32_e32 v90, v165, v165
	v_max_f32_e32 v157, v157, v157
	s_waitcnt lgkmcnt(11)
	v_max_f32_e32 v164, v164, v164
	v_max_f32_e32 v156, v156, v156
	v_max_f32_e32 v160, v160, v160
	v_max_f32_e32 v150, v150, v150
	s_waitcnt lgkmcnt(9)
	v_max_f32_e32 v158, v158, v158
	v_max_f32_e32 v148, v148, v148
	v_max_f32_e32 v151, v151, v151
	v_max_f32_e32 v30, v30, v30
	v_max_f32_e32 v149, v149, v149
	v_max_f32_e32 v29, v29, v29
	v_max_f32_e32 v144, v144, v144
	v_max_f32_e32 v26, v26, v26
	s_waitcnt lgkmcnt(8)
	v_max_f32_e32 v31, v31, v31
	v_max_f32_e32 v25, v25, v25
	v_max_f32_e32 v90, v157, v90
	s_waitcnt lgkmcnt(7)
	v_max_f32_e32 v157, v167, v167
	v_max_f32_e32 v161, v161, v161
	v_max_f32_e32 v156, v156, v164
	s_waitcnt lgkmcnt(3)
	v_max_f32_e32 v164, v166, v166
	v_max_f32_e32 v159, v159, v159
	v_max_f32_e32 v150, v150, v160
	v_max_f32_e32 v160, v163, v163
	v_max_f32_e32 v154, v154, v154
	v_max_f32_e32 v148, v148, v158
	s_waitcnt lgkmcnt(1)
	v_max_f32_e32 v158, v162, v162
	v_max_f32_e32 v152, v152, v152
	v_max_f32_e32 v30, v30, v151
	v_max_f32_e32 v151, v155, v155
	v_max_f32_e32 v145, v145, v145
	v_max_f32_e32 v29, v29, v149
	v_max_f32_e32 v149, v153, v153
	v_max_f32_e32 v143, v143, v143
	v_max_f32_e32 v26, v26, v144
	v_max_f32_e32 v144, v147, v147
	v_max_f32_e32 v28, v28, v28
	v_max_f32_e32 v25, v25, v31
	s_waitcnt lgkmcnt(0)
	v_max_f32_e32 v31, v146, v146
	v_max_f32_e32 v27, v27, v27
	v_max_f32_e32 v157, v161, v157
	v_max_f32_e32 v159, v159, v164
	v_max_f32_e32 v154, v154, v160
	v_max_f32_e32 v152, v152, v158
	v_max_f32_e32 v145, v145, v151
	v_max_f32_e32 v143, v143, v149
	v_max_f32_e32 v28, v28, v144
	v_max_f32_e32 v27, v27, v31
	v_min_f32_e32 v161, v90, v157
	v_min_f32_e32 v164, v156, v159
	v_min_f32_e32 v160, v150, v154
	v_min_f32_e32 v158, v148, v152
	v_min_f32_e32 v151, v30, v145
	v_min_f32_e32 v149, v29, v143
	v_min_f32_e32 v144, v26, v28
	v_min_f32_e32 v31, v25, v27
	v_max_f32_e32 v90, v90, v157
	v_max_f32_e32 v156, v156, v159
	v_max_f32_e32 v150, v150, v154
	v_max_f32_e32 v148, v148, v152
	v_max_f32_e32 v30, v30, v145
	v_max_f32_e32 v29, v29, v143
	v_max_f32_e32 v26, v26, v28
	v_max_f32_e32 v25, v25, v27
	v_min_f32_e32 v157, v90, v156
	v_min_f32_e32 v152, v150, v148
	v_min_f32_e32 v143, v30, v29
	v_min_f32_e32 v27, v26, v25
	v_max_f32_e32 v90, v90, v156
	v_max_f32_e32 v148, v150, v148
	v_max_f32_e32 v29, v30, v29
	v_max_f32_e32 v25, v26, v25
	v_min_f32_e32 v165, v161, v164
	v_min_f32_e32 v162, v160, v158
	v_min_f32_e32 v153, v151, v149
	v_min_f32_e32 v146, v144, v31
	v_max_f32_e32 v161, v161, v164
	v_max_f32_e32 v158, v160, v158
	v_max_f32_e32 v149, v151, v149
	v_max_f32_e32 v31, v144, v31
	v_min_f32_e32 v150, v90, v148
	v_min_f32_e32 v26, v29, v25
	v_max_f32_e32 v90, v90, v148
	v_max_f32_e32 v25, v29, v25
	v_min_f32_e32 v163, v165, v162
	v_min_f32_e32 v147, v153, v146
	v_max_f32_e32 v162, v165, v162
	v_max_f32_e32 v146, v153, v146
	v_min_f32_e32 v160, v161, v158
	v_min_f32_e32 v144, v149, v31
	v_max_f32_e32 v158, v161, v158
	v_max_f32_e32 v31, v149, v31
	v_min_f32_e32 v154, v157, v152
	v_min_f32_e32 v28, v143, v27
	v_max_f32_e32 v152, v157, v152
	v_max_f32_e32 v27, v143, v27
	v_min_f32_e32 v29, v90, v25
	v_max_f32_e32 v25, v90, v25
	v_min_f32_e32 v155, v163, v147
	v_max_f32_e32 v147, v163, v147
	v_min_f32_e32 v153, v162, v146
	v_max_f32_e32 v146, v162, v146
	v_min_f32_e32 v151, v160, v144
	v_max_f32_e32 v144, v160, v144
	v_min_f32_e32 v149, v158, v31
	v_max_f32_e32 v31, v158, v31
	v_min_f32_e32 v145, v154, v28
	v_max_f32_e32 v28, v154, v28
	v_min_f32_e32 v143, v152, v27
	v_max_f32_e32 v27, v152, v27
	v_min_f32_e32 v30, v150, v26
	v_max_f32_e32 v26, v150, v26
	ds_write2_b32 v16, v25, v29 offset1:1
	ds_write2_b32 v16, v26, v30 offset0:2 offset1:3
	ds_write2_b32 v16, v27, v143 offset0:4 offset1:5
	ds_write2_b32 v16, v28, v145 offset0:6 offset1:7
	ds_write2_b32 v16, v31, v149 offset0:8 offset1:9
	ds_write2_b32 v16, v144, v151 offset0:10 offset1:11
	ds_write2_b32 v16, v146, v153 offset0:12 offset1:13
	ds_write2_b32 v16, v147, v155 offset0:14 offset1:15
